# P4 epilogue residual loads pipelined (VGPR ring), P6 row scales hoisted, P8 v-phase wait counts, P4 tile order WGM 2
# speedup vs baseline: 1.0072x; 1.0072x over previous
; #define PG8_STAGE(bufoff, gbase, voff) do { _Pragma("unroll") for (int _i = 0; _i < 2; ++_i) \
;         __builtin_amdgcn_global_load_lds((const unsigned*)((const char*)(gbase) + (voff)[_i]), (PG8_LAS unsigned*)(lds + (bufoff) + ldsw + _i * 8192), 16, 0, 0); } while (0)
; #define PG8_BAR __builtin_amdgcn_s_barrier()
;     __host__ __device__ bool next(int i, Unit& u) const {
;         const long L = (long)i * G + c; if (L >= nwg) return false;
;         int wgid = (int)L; { const int q = nwg / NXCD, r = nwg % NXCD, xcd = wgid % NXCD, off = wgid / NXCD; wgid = (xcd < r ? xcd * (q + 1) : r * (q + 1) + (xcd - r) * q) + off; }
;         const int nig = WGM * nN, gid = wgid / nig, fm = gid * WGM, gsz = (nM - fm) < WGM ? (nM - fm) : WGM;
;         u.pm = fm + ((wgid % nig) % gsz); u.pn = (wgid % nig) / gsz; return true;
; template <class Epi, class Sched, bool ALIGN_EPI = false, bool SP2 = false>
; __device__ __forceinline__ void gemm_phase(PG8_LAS unsigned char* lds, const Gemm g, const Sched& S, const Epi& E) {
;     ...
;     const char* cA = (const char*)g.A + (size_t)cur.pm * tstep; const char* cB = (const char*)g.Bt + (size_t)cur.pn * tstep;
;     S.a_ready(cur);
;     if constexpr (SP2) {
;         PG8_STAGE(PG8_SB(0, 0), cB, voffB); PG8_STAGE(PG8_SB(0, 1), cB + hstep, voffB); PG8_STAGE(PG8_SA(0, 0), cA, voffA); PG8_STAGE(PG8_SA(0, 1), cA + hstep, voffA);
;         if (wr == 1) PG8_BAR;
.LBB0_551:
	v_lshrrev_b32_e32 v3, 1, v0
	v_and_b32_e32 v13, 24, v3
	v_lshrrev_b32_e32 v3, 5, v0
	v_lshlrev_b32_e32 v1, 4, v0
	v_and_b32_e32 v2, 32, v0
	v_and_b32_e32 v3, 4, v3
	v_bfe_u32 v4, v0, 2, 2
	v_bfe_u32 v12, v0, 2, 4
	v_bitop3_b32 v10, v1, v2, 48 bitop3:0x6c
	v_and_b32_e32 v11, 64, v0
	v_or3_b32 v3, v3, v4, v13
	v_lshrrev_b32_e32 v4, 3, v0
	v_or_b32_e32 v14, 0x2000, v1
	s_ashr_i32 s0, s2, 3
	v_or_b32_e32 v2, v10, v11
	v_and_or_b32 v5, v4, 48, v12
	v_and_or_b32 v4, v4, 32, v3
	v_lshrrev_b32_e32 v1, 7, v14
	s_movk_i32 s1, 0x70
	v_lshl_or_b32 v132, v4, 14, v2
	v_and_or_b32 v4, v1, s1, v12
	s_movk_i32 s1, 0x60
	s_add_i32 s0, s3, s0
	v_and_or_b32 v1, v1, s1, v3
	s_ashr_i32 s1, s0, 31
	s_lshr_b32 s1, s1, 27
	s_add_i32 s1, s0, s1
	s_ashr_i32 s3, s1, 5
	s_and_b32 s1, s1, 0xffffffe0
	s_sub_i32 s0, s0, s1
	s_bfe_i32 s1, s0, 0x80000
	s_bfe_u32 s1, s1, 0x1000c
	s_add_i32 s1, s0, s1
	s_bfe_i32 s4, s1, 0x80000
	s_and_b32 s1, s1, 0xfe
	s_sub_i32 s0, s0, s1
	s_lshl_b32 s3, s3, 1
	s_sext_i32_i16 s4, s4
	s_sext_i32_i8 s0, s0
	s_lshr_b32 s4, s4, 1
	s_add_i32 s26, s3, s0
	s_lshr_b32 s2, s5, 6
	s_ashr_i32 s27, s26, 31
	s_bfe_i64 s[10:11], s[4:5], 0x100000
	s_lshr_b32 s8, s5, 8
	s_lshl_b32 s36, s2, 10
	s_lshl_b64 s[0:1], s[26:27], 22
	s_lshl_b64 s[10:11], s[10:11], 22
	s_add_u32 s30, s56, s10
	s_addc_u32 s31, s57, s11
	s_add_i32 s27, s36, 0
	s_add_i32 m0, s27, 0x10000
	v_lshl_or_b32 v136, v1, 14, v2
	global_load_lds_dwordx4 v132, s[30:31]
	s_add_i32 m0, s27, 0x12000
	s_add_u32 s10, s30, 0x200000
	global_load_lds_dwordx4 v136, s[30:31]
	s_addc_u32 s11, s31, 0
	s_add_i32 m0, s27, 0x14000
	v_lshl_or_b32 v130, v5, 14, v2
	global_load_lds_dwordx4 v132, s[10:11]
	s_add_i32 m0, s27, 0x16000
	s_add_u32 s28, s64, s0
	s_addc_u32 s29, s65, s1
	s_add_i32 s37, s27, 0x2000
	global_load_lds_dwordx4 v136, s[10:11]
	s_mov_b32 m0, s27
	s_add_u32 s0, s28, 0x200000
	v_lshl_or_b32 v134, v4, 14, v2
	global_load_lds_dwordx4 v130, s[28:29]
	s_mov_b32 m0, s37
	s_addc_u32 s1, s29, 0
	s_add_i32 s38, s27, 0x4000
	global_load_lds_dwordx4 v134, s[28:29]
	s_mov_b32 m0, s38
	s_add_i32 s39, s27, 0x6000
	global_load_lds_dwordx4 v130, s[0:1]
	s_mov_b32 m0, s39
	v_mov_b32_e32 v133, 0
	global_load_lds_dwordx4 v134, s[0:1]
	v_mov_b32_e32 v137, v133
	v_mov_b32_e32 v131, v133
	v_mov_b32_e32 v135, v133
	s_cmp_eq_u32 s8, 1
	s_mov_b32 s40, 0
	v_lshl_add_u64 v[8:9], s[30:31], 0, v[132:133]
	v_lshl_add_u64 v[6:7], s[30:31], 0, v[136:137]
	v_lshl_add_u64 v[2:3], s[28:29], 0, v[130:131]
	s_cselect_b64 s[0:1], -1, 0
	s_cmp_lg_u32 s8, 1
	v_lshl_add_u64 v[4:5], s[28:29], 0, v[134:135]
	s_cbranch_scc1 .LBB0_553
	s_barrier

;     __host__ __device__ bool next(int i, Unit& u) const {
;         const long L = (long)i * G + c; if (L >= nwg) return false;
;         int wgid = (int)L; { const int q = nwg / NXCD, r = nwg % NXCD, xcd = wgid % NXCD, off = wgid / NXCD; wgid = (xcd < r ? xcd * (q + 1) : r * (q + 1) + (xcd - r) * q) + off; }
;         const int nig = WGM * nN, gid = wgid / nig, fm = gid * WGM, gsz = (nM - fm) < WGM ? (nM - fm) : WGM;
;         u.pm = fm + ((wgid % nig) % gsz); u.pn = (wgid % nig) / gsz; return true;
.LBB0_561:
	s_ashr_i32 s18, s20, 3
	s_add_i32 s18, s22, s18
	s_ashr_i32 s19, s18, 31
	s_lshr_b32 s19, s19, 27
	s_add_i32 s19, s18, s19
	s_ashr_i32 s20, s19, 5
	s_lshl_b32 s20, s20, 1
	s_sub_i32 s21, 64, s20
	s_min_i32 s21, s21, 2
	s_abs_i32 s22, s21
	v_cvt_f32_u32_e32 v2, s22
	s_sub_i32 s24, 0, s22
	s_and_b32 s19, s19, 0xffffffe0
	s_sub_i32 s19, s18, s19
	v_rcp_iflag_f32_e32 v2, v2
	s_abs_i32 s18, s19
	s_xor_b32 s23, s19, s21
	s_ashr_i32 s23, s23, 31
	v_mul_f32_e32 v2, 0x4f7ffffe, v2
	v_cvt_u32_f32_e32 v2, v2
	s_nop 0
	v_readfirstlane_b32 s25, v2
	s_mul_i32 s24, s24, s25
	s_mul_hi_u32 s24, s25, s24
	s_add_i32 s25, s25, s24
	s_mul_hi_u32 s24, s18, s25
	s_mul_i32 s25, s24, s22
	s_sub_i32 s18, s18, s25
	s_add_i32 s34, s24, 1
	s_sub_i32 s25, s18, s22
	s_cmp_ge_u32 s18, s22
	s_cselect_b32 s24, s34, s24
	s_cselect_b32 s18, s25, s18
	s_add_i32 s25, s24, 1
	s_cmp_ge_u32 s18, s22
	s_cselect_b32 s18, s25, s24
	s_xor_b32 s18, s18, s23
	s_sub_i32 s18, s18, s23
	s_mul_i32 s21, s18, s21
	s_sub_i32 s19, s19, s21
	s_add_i32 s20, s20, s19

.LBB0_838:
	s_add_i32 s54, s54, 2
	s_waitcnt vmcnt(32)
	v_cvt_pk_f32_fp8_e32 v[156:157], v124
	v_cvt_pk_f32_fp8_sdwa v[194:195], v124 src0_sel:WORD_1
	v_cvt_pk_f32_fp8_e32 v[196:197], v125
	v_cvt_pk_f32_fp8_sdwa v[124:125], v125 src0_sel:WORD_1
	v_lshl_add_u32 v128, v139, 2, s34
	s_waitcnt vmcnt(31)
	v_cvt_pk_f32_fp8_e32 v[204:205], v120
	v_cvt_pk_f32_fp8_sdwa v[206:207], v120 src0_sel:WORD_1
	v_cvt_pk_f32_fp8_e32 v[208:209], v121
	v_cvt_pk_f32_fp8_sdwa v[120:121], v121 src0_sel:WORD_1
	ds_read_b128 v[186:189], v128 offset:2048
	ds_read_b128 v[190:193], v128 offset:2064
	ds_read_b128 v[132:135], v128 offset:2080
	ds_read_b128 v[128:131], v128 offset:2096
	v_cvt_pk_f32_fp8_e32 v[198:199], v126
	s_waitcnt lgkmcnt(3)
	v_pk_fma_f32 v[156:157], v[186:187], v[156:157], 0 op_sel_hi:[0,1,0]
	v_pk_fma_f32 v[194:195], v[186:187], v[194:195], 0 op_sel_hi:[0,1,0]
	v_pk_fma_f32 v[124:125], v[186:187], v[124:125], 0 op_sel_hi:[0,1,0]
	v_cvt_pk_f32_fp8_sdwa v[200:201], v126 src0_sel:WORD_1
	v_cvt_pk_f32_fp8_e32 v[202:203], v127
	v_cvt_pk_f32_fp8_sdwa v[126:127], v127 src0_sel:WORD_1
	v_pk_fma_f32 v[156:157], v[186:187], v[204:205], v[156:157] op_sel:[1,0,0]
	v_pk_fma_f32 v[194:195], v[186:187], v[206:207], v[194:195] op_sel:[1,0,0]
	v_pk_fma_f32 v[120:121], v[186:187], v[120:121], v[124:125] op_sel:[1,0,0]
	v_cvt_pk_f32_fp8_e32 v[124:125], v122
	v_cvt_pk_f32_fp8_sdwa v[204:205], v122 src0_sel:WORD_1
	v_cvt_pk_f32_fp8_e32 v[206:207], v123
	v_cvt_pk_f32_fp8_sdwa v[122:123], v123 src0_sel:WORD_1
	v_pk_fma_f32 v[196:197], v[186:187], v[196:197], 0 op_sel_hi:[0,1,0]
	v_pk_fma_f32 v[198:199], v[186:187], v[198:199], 0 op_sel_hi:[0,1,0]
	v_pk_fma_f32 v[200:201], v[186:187], v[200:201], 0 op_sel_hi:[0,1,0]
	v_pk_fma_f32 v[202:203], v[186:187], v[202:203], 0 op_sel_hi:[0,1,0]
	v_pk_fma_f32 v[126:127], v[186:187], v[126:127], 0 op_sel_hi:[0,1,0]
	v_pk_fma_f32 v[196:197], v[186:187], v[208:209], v[196:197] op_sel:[1,0,0]
	v_pk_fma_f32 v[124:125], v[186:187], v[124:125], v[198:199] op_sel:[1,0,0]
	v_pk_fma_f32 v[198:199], v[186:187], v[204:205], v[200:201] op_sel:[1,0,0]
	v_pk_fma_f32 v[200:201], v[186:187], v[206:207], v[202:203] op_sel:[1,0,0]
	v_pk_fma_f32 v[122:123], v[186:187], v[122:123], v[126:127] op_sel:[1,0,0]
	s_waitcnt vmcnt(30)
	v_cvt_pk_f32_fp8_e32 v[126:127], v116
	v_cvt_pk_f32_fp8_sdwa v[186:187], v116 src0_sel:WORD_1
	v_cvt_pk_f32_fp8_e32 v[202:203], v117
	v_cvt_pk_f32_fp8_sdwa v[116:117], v117 src0_sel:WORD_1
	v_pk_fma_f32 v[126:127], v[188:189], v[126:127], v[156:157] op_sel_hi:[0,1,1]
	v_pk_fma_f32 v[156:157], v[188:189], v[186:187], v[194:195] op_sel_hi:[0,1,1]
	v_pk_fma_f32 v[186:187], v[188:189], v[202:203], v[196:197] op_sel_hi:[0,1,1]
	v_pk_fma_f32 v[116:117], v[188:189], v[116:117], v[120:121] op_sel_hi:[0,1,1]
	v_cvt_pk_f32_fp8_e32 v[120:121], v118
	v_cvt_pk_f32_fp8_sdwa v[194:195], v118 src0_sel:WORD_1
	v_cvt_pk_f32_fp8_e32 v[196:197], v119
	v_cvt_pk_f32_fp8_sdwa v[118:119], v119 src0_sel:WORD_1
	v_pk_fma_f32 v[120:121], v[188:189], v[120:121], v[124:125] op_sel_hi:[0,1,1]
	v_pk_fma_f32 v[124:125], v[188:189], v[194:195], v[198:199] op_sel_hi:[0,1,1]
	v_pk_fma_f32 v[194:195], v[188:189], v[196:197], v[200:201] op_sel_hi:[0,1,1]
	v_pk_fma_f32 v[118:119], v[188:189], v[118:119], v[122:123] op_sel_hi:[0,1,1]
	v_mov_b32_e32 v122, v189
	s_waitcnt vmcnt(29)
	v_cvt_pk_f32_fp8_e32 v[188:189], v112
	v_cvt_pk_f32_fp8_sdwa v[196:197], v112 src0_sel:WORD_1
	v_cvt_pk_f32_fp8_e32 v[198:199], v113
	v_cvt_pk_f32_fp8_sdwa v[112:113], v113 src0_sel:WORD_1
	v_pk_fma_f32 v[126:127], v[122:123], v[188:189], v[126:127] op_sel_hi:[0,1,1]
	v_pk_fma_f32 v[156:157], v[122:123], v[196:197], v[156:157] op_sel_hi:[0,1,1]
	v_cvt_pk_f32_fp8_sdwa v[188:189], v114 src0_sel:WORD_1
	v_pk_fma_f32 v[112:113], v[122:123], v[112:113], v[116:117] op_sel_hi:[0,1,1]
	v_cvt_pk_f32_fp8_e32 v[116:117], v114
	v_cvt_pk_f32_fp8_e32 v[196:197], v115
	v_cvt_pk_f32_fp8_sdwa v[114:115], v115 src0_sel:WORD_1
	v_pk_fma_f32 v[186:187], v[122:123], v[198:199], v[186:187] op_sel_hi:[0,1,1]
	v_pk_fma_f32 v[116:117], v[122:123], v[116:117], v[120:121] op_sel_hi:[0,1,1]
	v_pk_fma_f32 v[120:121], v[122:123], v[188:189], v[124:125] op_sel_hi:[0,1,1]
	v_pk_fma_f32 v[124:125], v[122:123], v[196:197], v[194:195] op_sel_hi:[0,1,1]
	v_pk_fma_f32 v[114:115], v[122:123], v[114:115], v[118:119] op_sel_hi:[0,1,1]
	s_waitcnt vmcnt(28)
	v_cvt_pk_f32_fp8_e32 v[118:119], v108
	v_cvt_pk_f32_fp8_sdwa v[122:123], v108 src0_sel:WORD_1
	v_cvt_pk_f32_fp8_e32 v[188:189], v109
	v_cvt_pk_f32_fp8_sdwa v[108:109], v109 src0_sel:WORD_1
	s_waitcnt lgkmcnt(2)
	v_pk_fma_f32 v[118:119], v[190:191], v[118:119], v[126:127] op_sel_hi:[0,1,1]
	v_pk_fma_f32 v[122:123], v[190:191], v[122:123], v[156:157] op_sel_hi:[0,1,1]
	v_pk_fma_f32 v[126:127], v[190:191], v[188:189], v[186:187] op_sel_hi:[0,1,1]
	v_pk_fma_f32 v[108:109], v[190:191], v[108:109], v[112:113] op_sel_hi:[0,1,1]
	v_cvt_pk_f32_fp8_e32 v[112:113], v110
	v_cvt_pk_f32_fp8_sdwa v[156:157], v110 src0_sel:WORD_1
	v_cvt_pk_f32_fp8_e32 v[186:187], v111
	v_cvt_pk_f32_fp8_sdwa v[110:111], v111 src0_sel:WORD_1
	v_pk_fma_f32 v[112:113], v[190:191], v[112:113], v[116:117] op_sel_hi:[0,1,1]
	v_pk_fma_f32 v[116:117], v[190:191], v[156:157], v[120:121] op_sel_hi:[0,1,1]
	v_pk_fma_f32 v[120:121], v[190:191], v[186:187], v[124:125] op_sel_hi:[0,1,1]
	v_pk_fma_f32 v[110:111], v[190:191], v[110:111], v[114:115] op_sel_hi:[0,1,1]
	s_waitcnt vmcnt(27)
	v_cvt_pk_f32_fp8_e32 v[114:115], v104
	v_cvt_pk_f32_fp8_sdwa v[124:125], v104 src0_sel:WORD_1
	v_cvt_pk_f32_fp8_e32 v[156:157], v105
	v_cvt_pk_f32_fp8_sdwa v[104:105], v105 src0_sel:WORD_1
	v_pk_fma_f32 v[114:115], v[190:191], v[114:115], v[118:119] op_sel:[1,0,0]
	v_pk_fma_f32 v[118:119], v[190:191], v[124:125], v[122:123] op_sel:[1,0,0]
	v_pk_fma_f32 v[122:123], v[190:191], v[156:157], v[126:127] op_sel:[1,0,0]
	v_pk_fma_f32 v[104:105], v[190:191], v[104:105], v[108:109] op_sel:[1,0,0]
	v_cvt_pk_f32_fp8_e32 v[108:109], v106
	v_cvt_pk_f32_fp8_sdwa v[124:125], v106 src0_sel:WORD_1
	v_cvt_pk_f32_fp8_e32 v[126:127], v107
	v_cvt_pk_f32_fp8_sdwa v[106:107], v107 src0_sel:WORD_1
	v_pk_fma_f32 v[108:109], v[190:191], v[108:109], v[112:113] op_sel:[1,0,0]
	v_pk_fma_f32 v[112:113], v[190:191], v[124:125], v[116:117] op_sel:[1,0,0]
	v_pk_fma_f32 v[116:117], v[190:191], v[126:127], v[120:121] op_sel:[1,0,0]
	v_pk_fma_f32 v[106:107], v[190:191], v[106:107], v[110:111] op_sel:[1,0,0]
	s_waitcnt vmcnt(26)
	v_cvt_pk_f32_fp8_e32 v[110:111], v100
	v_cvt_pk_f32_fp8_sdwa v[120:121], v100 src0_sel:WORD_1
	v_cvt_pk_f32_fp8_e32 v[124:125], v101
	v_cvt_pk_f32_fp8_sdwa v[100:101], v101 src0_sel:WORD_1
	v_pk_fma_f32 v[110:111], v[192:193], v[110:111], v[114:115] op_sel_hi:[0,1,1]
	v_pk_fma_f32 v[114:115], v[192:193], v[120:121], v[118:119] op_sel_hi:[0,1,1]
	v_pk_fma_f32 v[118:119], v[192:193], v[124:125], v[122:123] op_sel_hi:[0,1,1]
	v_pk_fma_f32 v[100:101], v[192:193], v[100:101], v[104:105] op_sel_hi:[0,1,1]
	v_cvt_pk_f32_fp8_e32 v[104:105], v102
	v_cvt_pk_f32_fp8_sdwa v[120:121], v102 src0_sel:WORD_1
	v_cvt_pk_f32_fp8_e32 v[122:123], v103
	v_cvt_pk_f32_fp8_sdwa v[102:103], v103 src0_sel:WORD_1
	v_pk_fma_f32 v[104:105], v[192:193], v[104:105], v[108:109] op_sel_hi:[0,1,1]
	v_pk_fma_f32 v[108:109], v[192:193], v[120:121], v[112:113] op_sel_hi:[0,1,1]
	v_pk_fma_f32 v[112:113], v[192:193], v[122:123], v[116:117] op_sel_hi:[0,1,1]
	s_waitcnt vmcnt(25)
	v_cvt_pk_f32_fp8_e32 v[116:117], v96
	v_cvt_pk_f32_fp8_sdwa v[120:121], v96 src0_sel:WORD_1
	v_cvt_pk_f32_fp8_e32 v[122:123], v97
	v_cvt_pk_f32_fp8_sdwa v[96:97], v97 src0_sel:WORD_1
	v_pk_fma_f32 v[102:103], v[192:193], v[102:103], v[106:107] op_sel_hi:[0,1,1]
	v_mov_b32_e32 v106, v193
	v_pk_fma_f32 v[110:111], v[106:107], v[116:117], v[110:111] op_sel_hi:[0,1,1]
	v_pk_fma_f32 v[114:115], v[106:107], v[120:121], v[114:115] op_sel_hi:[0,1,1]
	v_pk_fma_f32 v[116:117], v[106:107], v[122:123], v[118:119] op_sel_hi:[0,1,1]
	v_pk_fma_f32 v[96:97], v[106:107], v[96:97], v[100:101] op_sel_hi:[0,1,1]
	v_cvt_pk_f32_fp8_e32 v[100:101], v98
	v_cvt_pk_f32_fp8_sdwa v[118:119], v98 src0_sel:WORD_1
	v_cvt_pk_f32_fp8_e32 v[120:121], v99
	v_cvt_pk_f32_fp8_sdwa v[98:99], v99 src0_sel:WORD_1
	v_pk_fma_f32 v[100:101], v[106:107], v[100:101], v[104:105] op_sel_hi:[0,1,1]
	v_pk_fma_f32 v[104:105], v[106:107], v[118:119], v[108:109] op_sel_hi:[0,1,1]
	v_pk_fma_f32 v[108:109], v[106:107], v[120:121], v[112:113] op_sel_hi:[0,1,1]
	v_pk_fma_f32 v[98:99], v[106:107], v[98:99], v[102:103] op_sel_hi:[0,1,1]
	s_waitcnt vmcnt(24)
	v_cvt_pk_f32_fp8_e32 v[102:103], v92
	v_cvt_pk_f32_fp8_sdwa v[106:107], v92 src0_sel:WORD_1
	v_cvt_pk_f32_fp8_e32 v[112:113], v93
	v_cvt_pk_f32_fp8_sdwa v[92:93], v93 src0_sel:WORD_1
	s_waitcnt lgkmcnt(1)
	v_pk_fma_f32 v[102:103], v[132:133], v[102:103], v[110:111] op_sel_hi:[0,1,1]
	v_pk_fma_f32 v[106:107], v[132:133], v[106:107], v[114:115] op_sel_hi:[0,1,1]
	v_pk_fma_f32 v[110:111], v[132:133], v[112:113], v[116:117] op_sel_hi:[0,1,1]
	v_pk_fma_f32 v[92:93], v[132:133], v[92:93], v[96:97] op_sel_hi:[0,1,1]
	v_cvt_pk_f32_fp8_e32 v[96:97], v94
	v_cvt_pk_f32_fp8_sdwa v[112:113], v94 src0_sel:WORD_1
	v_cvt_pk_f32_fp8_e32 v[114:115], v95
	v_cvt_pk_f32_fp8_sdwa v[94:95], v95 src0_sel:WORD_1
	v_pk_fma_f32 v[96:97], v[132:133], v[96:97], v[100:101] op_sel_hi:[0,1,1]
	v_pk_fma_f32 v[100:101], v[132:133], v[112:113], v[104:105] op_sel_hi:[0,1,1]
	v_pk_fma_f32 v[104:105], v[132:133], v[114:115], v[108:109] op_sel_hi:[0,1,1]
	v_pk_fma_f32 v[94:95], v[132:133], v[94:95], v[98:99] op_sel_hi:[0,1,1]
	s_waitcnt vmcnt(23)
	v_cvt_pk_f32_fp8_e32 v[98:99], v88
	v_cvt_pk_f32_fp8_sdwa v[108:109], v88 src0_sel:WORD_1
	v_cvt_pk_f32_fp8_e32 v[112:113], v89
	v_cvt_pk_f32_fp8_sdwa v[88:89], v89 src0_sel:WORD_1
	v_pk_fma_f32 v[98:99], v[132:133], v[98:99], v[102:103] op_sel:[1,0,0]
	v_pk_fma_f32 v[102:103], v[132:133], v[108:109], v[106:107] op_sel:[1,0,0]
	v_pk_fma_f32 v[106:107], v[132:133], v[112:113], v[110:111] op_sel:[1,0,0]
	v_pk_fma_f32 v[88:89], v[132:133], v[88:89], v[92:93] op_sel:[1,0,0]
	v_cvt_pk_f32_fp8_e32 v[92:93], v90
	v_cvt_pk_f32_fp8_sdwa v[108:109], v90 src0_sel:WORD_1
	v_cvt_pk_f32_fp8_e32 v[110:111], v91
	v_cvt_pk_f32_fp8_sdwa v[90:91], v91 src0_sel:WORD_1
	v_pk_fma_f32 v[92:93], v[132:133], v[92:93], v[96:97] op_sel:[1,0,0]
	v_pk_fma_f32 v[96:97], v[132:133], v[108:109], v[100:101] op_sel:[1,0,0]
	v_pk_fma_f32 v[100:101], v[132:133], v[110:111], v[104:105] op_sel:[1,0,0]
	v_pk_fma_f32 v[90:91], v[132:133], v[90:91], v[94:95] op_sel:[1,0,0]
	s_waitcnt vmcnt(22)
	v_cvt_pk_f32_fp8_e32 v[94:95], v84
	v_cvt_pk_f32_fp8_sdwa v[104:105], v84 src0_sel:WORD_1
	v_cvt_pk_f32_fp8_e32 v[108:109], v85
	v_cvt_pk_f32_fp8_sdwa v[84:85], v85 src0_sel:WORD_1
	v_pk_fma_f32 v[94:95], v[134:135], v[94:95], v[98:99] op_sel_hi:[0,1,1]
	v_pk_fma_f32 v[98:99], v[134:135], v[104:105], v[102:103] op_sel_hi:[0,1,1]
	v_pk_fma_f32 v[102:103], v[134:135], v[108:109], v[106:107] op_sel_hi:[0,1,1]
	v_pk_fma_f32 v[84:85], v[134:135], v[84:85], v[88:89] op_sel_hi:[0,1,1]
	v_cvt_pk_f32_fp8_e32 v[88:89], v86
	v_cvt_pk_f32_fp8_sdwa v[104:105], v86 src0_sel:WORD_1
	v_cvt_pk_f32_fp8_e32 v[106:107], v87
	v_cvt_pk_f32_fp8_sdwa v[86:87], v87 src0_sel:WORD_1
	v_pk_fma_f32 v[88:89], v[134:135], v[88:89], v[92:93] op_sel_hi:[0,1,1]
	v_pk_fma_f32 v[92:93], v[134:135], v[104:105], v[96:97] op_sel_hi:[0,1,1]
	v_pk_fma_f32 v[96:97], v[134:135], v[106:107], v[100:101] op_sel_hi:[0,1,1]
	s_waitcnt vmcnt(21)
; __device__ __forceinline__ void rs16(const float (&d)[16], int bit, int sh1, int sh2, int sh3, float (&out)[2]) {
;     float n8[8], n4[4];
; #pragma unroll
;     for (int m = 0; m < 8; ++m) { const bool up = (bit & sh1) != 0; const float mine = up ? d[8 + m] : d[m], theirs = up ? d[m] : d[8 + m]; n8[m] = mine + __shfl_xor(theirs, sh1); }
	v_cvt_pk_f32_fp8_e32 v[100:101], v80
	v_cvt_pk_f32_fp8_sdwa v[104:105], v80 src0_sel:WORD_1
	v_cvt_pk_f32_fp8_e32 v[106:107], v81
	v_cvt_pk_f32_fp8_sdwa v[80:81], v81 src0_sel:WORD_1
	v_pk_fma_f32 v[86:87], v[134:135], v[86:87], v[90:91] op_sel_hi:[0,1,1]
	v_mov_b32_e32 v90, v135
	v_pk_fma_f32 v[94:95], v[90:91], v[100:101], v[94:95] op_sel_hi:[0,1,1]
	v_pk_fma_f32 v[98:99], v[90:91], v[104:105], v[98:99] op_sel_hi:[0,1,1]
	v_pk_fma_f32 v[100:101], v[90:91], v[106:107], v[102:103] op_sel_hi:[0,1,1]
	v_pk_fma_f32 v[80:81], v[90:91], v[80:81], v[84:85] op_sel_hi:[0,1,1]
	v_cvt_pk_f32_fp8_e32 v[84:85], v82
	v_cvt_pk_f32_fp8_sdwa v[102:103], v82 src0_sel:WORD_1
	v_cvt_pk_f32_fp8_e32 v[104:105], v83
	v_cvt_pk_f32_fp8_sdwa v[82:83], v83 src0_sel:WORD_1
	v_pk_fma_f32 v[84:85], v[90:91], v[84:85], v[88:89] op_sel_hi:[0,1,1]
	v_pk_fma_f32 v[88:89], v[90:91], v[102:103], v[92:93] op_sel_hi:[0,1,1]
	v_pk_fma_f32 v[92:93], v[90:91], v[104:105], v[96:97] op_sel_hi:[0,1,1]
	v_pk_fma_f32 v[82:83], v[90:91], v[82:83], v[86:87] op_sel_hi:[0,1,1]
	s_waitcnt vmcnt(20)
	v_cvt_pk_f32_fp8_e32 v[86:87], v76
	v_cvt_pk_f32_fp8_sdwa v[90:91], v76 src0_sel:WORD_1
	v_cvt_pk_f32_fp8_e32 v[96:97], v77
	v_cvt_pk_f32_fp8_sdwa v[76:77], v77 src0_sel:WORD_1
	s_waitcnt lgkmcnt(0)
	v_pk_fma_f32 v[86:87], v[128:129], v[86:87], v[94:95] op_sel_hi:[0,1,1]
	v_pk_fma_f32 v[90:91], v[128:129], v[90:91], v[98:99] op_sel_hi:[0,1,1]
	v_pk_fma_f32 v[94:95], v[128:129], v[96:97], v[100:101] op_sel_hi:[0,1,1]
	v_pk_fma_f32 v[76:77], v[128:129], v[76:77], v[80:81] op_sel_hi:[0,1,1]
	v_cvt_pk_f32_fp8_e32 v[80:81], v78
	v_cvt_pk_f32_fp8_sdwa v[96:97], v78 src0_sel:WORD_1
	v_cvt_pk_f32_fp8_e32 v[98:99], v79
	v_cvt_pk_f32_fp8_sdwa v[78:79], v79 src0_sel:WORD_1
	v_pk_fma_f32 v[80:81], v[128:129], v[80:81], v[84:85] op_sel_hi:[0,1,1]
	v_pk_fma_f32 v[84:85], v[128:129], v[96:97], v[88:89] op_sel_hi:[0,1,1]
	v_pk_fma_f32 v[88:89], v[128:129], v[98:99], v[92:93] op_sel_hi:[0,1,1]
	v_pk_fma_f32 v[78:79], v[128:129], v[78:79], v[82:83] op_sel_hi:[0,1,1]
	s_waitcnt vmcnt(19)
	v_cvt_pk_f32_fp8_e32 v[82:83], v72
	v_cvt_pk_f32_fp8_sdwa v[92:93], v72 src0_sel:WORD_1
	v_cvt_pk_f32_fp8_e32 v[96:97], v73
	v_cvt_pk_f32_fp8_sdwa v[72:73], v73 src0_sel:WORD_1
	v_pk_fma_f32 v[82:83], v[128:129], v[82:83], v[86:87] op_sel:[1,0,0]
	v_pk_fma_f32 v[86:87], v[128:129], v[92:93], v[90:91] op_sel:[1,0,0]
	v_pk_fma_f32 v[90:91], v[128:129], v[96:97], v[94:95] op_sel:[1,0,0]
	v_pk_fma_f32 v[72:73], v[128:129], v[72:73], v[76:77] op_sel:[1,0,0]
	v_cvt_pk_f32_fp8_e32 v[76:77], v74
	v_cvt_pk_f32_fp8_sdwa v[92:93], v74 src0_sel:WORD_1
	v_cvt_pk_f32_fp8_e32 v[94:95], v75
	v_cvt_pk_f32_fp8_sdwa v[74:75], v75 src0_sel:WORD_1
	v_pk_fma_f32 v[76:77], v[128:129], v[76:77], v[80:81] op_sel:[1,0,0]
	v_pk_fma_f32 v[80:81], v[128:129], v[92:93], v[84:85] op_sel:[1,0,0]
	v_pk_fma_f32 v[84:85], v[128:129], v[94:95], v[88:89] op_sel:[1,0,0]
	v_pk_fma_f32 v[74:75], v[128:129], v[74:75], v[78:79] op_sel:[1,0,0]
	s_waitcnt vmcnt(18)
	v_cvt_pk_f32_fp8_e32 v[78:79], v68
	v_cvt_pk_f32_fp8_sdwa v[88:89], v68 src0_sel:WORD_1
	v_cvt_pk_f32_fp8_e32 v[92:93], v69
	v_cvt_pk_f32_fp8_sdwa v[68:69], v69 src0_sel:WORD_1
	v_pk_fma_f32 v[78:79], v[130:131], v[78:79], v[82:83] op_sel_hi:[0,1,1]
	v_pk_fma_f32 v[82:83], v[130:131], v[88:89], v[86:87] op_sel_hi:[0,1,1]
	v_pk_fma_f32 v[86:87], v[130:131], v[92:93], v[90:91] op_sel_hi:[0,1,1]
	v_pk_fma_f32 v[68:69], v[130:131], v[68:69], v[72:73] op_sel_hi:[0,1,1]
	v_cvt_pk_f32_fp8_e32 v[72:73], v70
	v_cvt_pk_f32_fp8_sdwa v[88:89], v70 src0_sel:WORD_1
	v_cvt_pk_f32_fp8_e32 v[90:91], v71
	v_cvt_pk_f32_fp8_sdwa v[70:71], v71 src0_sel:WORD_1
	v_pk_fma_f32 v[72:73], v[130:131], v[72:73], v[76:77] op_sel_hi:[0,1,1]
	v_pk_fma_f32 v[76:77], v[130:131], v[88:89], v[80:81] op_sel_hi:[0,1,1]
	v_pk_fma_f32 v[80:81], v[130:131], v[90:91], v[84:85] op_sel_hi:[0,1,1]
	s_waitcnt vmcnt(17)
	v_cvt_pk_f32_fp8_e32 v[84:85], v64
	v_cvt_pk_f32_fp8_sdwa v[88:89], v64 src0_sel:WORD_1
	v_cvt_pk_f32_fp8_e32 v[90:91], v65
	v_cvt_pk_f32_fp8_sdwa v[64:65], v65 src0_sel:WORD_1
	v_pk_fma_f32 v[70:71], v[130:131], v[70:71], v[74:75] op_sel_hi:[0,1,1]
	v_mov_b32_e32 v74, v131
	v_pk_fma_f32 v[78:79], v[74:75], v[84:85], v[78:79] op_sel_hi:[0,1,1]
	v_pk_fma_f32 v[64:65], v[74:75], v[64:65], v[68:69] op_sel_hi:[0,1,1]
	v_cvt_pk_f32_fp8_e32 v[68:69], v66
	v_pk_fma_f32 v[82:83], v[74:75], v[88:89], v[82:83] op_sel_hi:[0,1,1]
	v_pk_fma_f32 v[84:85], v[74:75], v[90:91], v[86:87] op_sel_hi:[0,1,1]
	v_cvt_pk_f32_fp8_sdwa v[86:87], v66 src0_sel:WORD_1
	v_cvt_pk_f32_fp8_e32 v[88:89], v67
	v_cvt_pk_f32_fp8_sdwa v[66:67], v67 src0_sel:WORD_1
	v_pk_fma_f32 v[68:69], v[74:75], v[68:69], v[72:73] op_sel_hi:[0,1,1]
	v_pk_fma_f32 v[72:73], v[74:75], v[86:87], v[76:77] op_sel_hi:[0,1,1]
	v_pk_fma_f32 v[76:77], v[74:75], v[88:89], v[80:81] op_sel_hi:[0,1,1]
	v_pk_fma_f32 v[66:67], v[74:75], v[66:67], v[70:71] op_sel_hi:[0,1,1]
	v_cndmask_b32_e64 v70, v68, v78, s[8:9]
	v_cndmask_b32_e64 v68, v78, v68, s[8:9]
	ds_bpermute_b32 v68, v137, v68
	v_cndmask_b32_e64 v71, v79, v69, s[8:9]
	ds_bpermute_b32 v71, v137, v71
	v_cndmask_b32_e64 v74, v82, v72, s[8:9]
	ds_bpermute_b32 v74, v137, v74
	s_waitcnt lgkmcnt(2)
	v_add_f32_e32 v68, v70, v68
	v_cndmask_b32_e64 v69, v69, v79, s[8:9]
	v_cndmask_b32_e64 v70, v72, v82, s[8:9]
	v_cndmask_b32_e64 v72, v83, v73, s[8:9]
	s_waitcnt lgkmcnt(1)
	v_add_f32_e32 v69, v69, v71
	v_cndmask_b32_e64 v71, v73, v83, s[8:9]
	ds_bpermute_b32 v72, v137, v72
	v_cndmask_b32_e64 v73, v84, v76, s[8:9]
	s_waitcnt lgkmcnt(1)
	v_add_f32_e32 v70, v70, v74
	ds_bpermute_b32 v73, v137, v73
	v_cndmask_b32_e64 v74, v85, v77, s[8:9]
	ds_bpermute_b32 v74, v137, v74
	s_waitcnt lgkmcnt(2)
; __device__ __forceinline__ void peer_block(LAS unsigned char* wl, int tok0, const unsigned char* XQ, const float* XS, const unsigned char* U8, const unsigned char* V8, const float* SU, const float* SV, const int* IDX, const float* GATE, const bf16* HB, float* HO, bf16* X2, const float* wfin, int lan ...
;     ...
;     {   u32x4 bufA[16], bufB[16];
;         PB_LOAD(bufA, V8, 0);
; #pragma unroll 1
;         for (int it = 0; it < 256; it += 2) {
;             PB_LOAD(bufB, V8, it + 1);
;             __builtin_amdgcn_sched_barrier(0);
;             PB_VCOMP(bufA, it);
;             __builtin_amdgcn_sched_barrier(0);
;             if (it + 2 < 256) { PB_LOAD(bufA, V8, it + 2); }
;             __builtin_amdgcn_sched_barrier(0);
;             PB_VCOMP(bufB, it + 1);
;             __builtin_amdgcn_sched_barrier(0);
	v_add_f32_e32 v71, v71, v72
	v_cndmask_b32_e64 v72, v76, v84, s[8:9]
	s_waitcnt lgkmcnt(1)
	v_add_f32_e32 v72, v72, v73
	v_cndmask_b32_e64 v73, v77, v85, s[8:9]
	s_waitcnt lgkmcnt(0)
	v_add_f32_e32 v73, v73, v74
	v_cndmask_b32_e64 v74, v66, v64, s[8:9]
	v_cndmask_b32_e64 v64, v64, v66, s[8:9]
	v_cndmask_b32_e64 v66, v65, v67, s[8:9]
	ds_bpermute_b32 v64, v137, v64
	ds_bpermute_b32 v66, v137, v66
	v_cndmask_b32_e64 v65, v67, v65, s[8:9]
	v_cndmask_b32_e64 v75, v68, v72, s[10:11]
	v_cndmask_b32_e64 v67, v73, v69, s[10:11]
	s_waitcnt lgkmcnt(1)
	v_add_f32_e32 v64, v74, v64
	s_waitcnt lgkmcnt(0)
	v_add_f32_e32 v65, v65, v66
	v_cndmask_b32_e64 v66, v72, v68, s[10:11]
	v_cndmask_b32_e64 v68, v69, v73, s[10:11]
	v_cndmask_b32_e64 v69, v70, v64, s[10:11]
	v_cndmask_b32_e64 v72, v71, v65, s[10:11]
	ds_bpermute_b32 v75, v138, v75
	ds_bpermute_b32 v68, v138, v68
	ds_bpermute_b32 v69, v138, v69
	ds_bpermute_b32 v72, v138, v72
	v_cndmask_b32_e64 v64, v64, v70, s[10:11]
	v_cndmask_b32_e64 v65, v65, v71, s[10:11]
	s_waitcnt lgkmcnt(3)
	v_add_f32_e32 v66, v66, v75
	s_waitcnt lgkmcnt(2)
	v_add_f32_e32 v67, v67, v68
	s_waitcnt lgkmcnt(1)
	v_add_f32_e32 v64, v64, v69
	s_waitcnt lgkmcnt(0)
	v_add_f32_e32 v65, v65, v72
	v_cndmask_b32_e64 v68, v66, v64, s[12:13]
	v_cndmask_b32_e64 v69, v67, v65, s[12:13]
	s_or_b32 s56, s56, s2
	ds_bpermute_b32 v68, v136, v68
	ds_bpermute_b32 v69, v136, v69
	s_ashr_i32 s57, s56, 31
	s_lshl_b64 s[56:57], s[56:57], 13
	s_add_u32 s56, s64, s56
	s_addc_u32 s57, s65, s57
	s_lshl_b32 s55, s55, 8
	v_cndmask_b32_e64 v64, v64, v66, s[12:13]
	v_cndmask_b32_e64 v65, v65, v67, s[12:13]
	s_add_u32 s56, s56, s55
	s_waitcnt lgkmcnt(1)
	v_add_f32_e32 v64, v64, v68
	s_waitcnt lgkmcnt(0)
	v_add_f32_e32 v65, v65, v69
	s_addc_u32 s57, s57, 0
	v_cvt_pk_bf16_f32 v66, v64, v65
	v_lshl_add_u64 v[64:65], s[56:57], 0, v[140:141]
	v_lshl_add_u64 v[64:65], v[64:65], 0, v[154:155]
	global_store_dword v[64:65], v66, off
	s_add_i32 s3, s3, 16
	s_add_i32 s22, s22, 0x80000
	s_add_i32 s53, s53, 32
	s_and_b64 vcc, exec, s[30:31]
	s_cbranch_vccnz .LBB0_841
.LBB0_839:
	s_and_b32 s30, s54, 6
	s_or_b32 s56, s30, 1
	v_lshl_or_b32 v139, s56, 7, v163
	v_lshl_add_u32 v68, v139, 1, s34
	ds_read_b128 v[64:67], v68
	s_lshr_b32 s55, s54, 3
	s_lshl_b32 s31, s55, 21
	s_add_u32 s58, s14, s31
	s_addc_u32 s59, s15, 0
	s_waitcnt lgkmcnt(0)
	v_lshlrev_b32_e32 v72, 7, v64
	v_bfe_u32 v64, v64, 16, 16
	v_and_or_b32 v72, v72, s36, v142
	v_lshl_or_b32 v64, v64, 7, v142
	ds_read_b128 v[68:71], v68 offset:16
	global_load_dwordx4 v[124:127], v72, s[58:59]
	global_load_dwordx4 v[120:123], v64, s[58:59]
	v_lshlrev_b32_e32 v64, 7, v65
	v_bfe_u32 v65, v65, 16, 16
	v_and_or_b32 v64, v64, s36, v142
	v_lshl_or_b32 v65, v65, 7, v142
	global_load_dwordx4 v[116:119], v64, s[58:59]
	global_load_dwordx4 v[112:115], v65, s[58:59]
	v_lshlrev_b32_e32 v64, 7, v66
	v_bfe_u32 v65, v66, 16, 16
	v_and_or_b32 v64, v64, s36, v142
	v_lshl_or_b32 v65, v65, 7, v142
	global_load_dwordx4 v[108:111], v64, s[58:59]
	global_load_dwordx4 v[104:107], v65, s[58:59]
	v_lshlrev_b32_e32 v64, 7, v67
	v_bfe_u32 v65, v67, 16, 16
	v_and_or_b32 v64, v64, s36, v142
	v_lshl_or_b32 v65, v65, 7, v142
	global_load_dwordx4 v[100:103], v64, s[58:59]
	global_load_dwordx4 v[96:99], v65, s[58:59]
	s_waitcnt lgkmcnt(0)
	v_lshlrev_b32_e32 v64, 7, v68
	v_bfe_u32 v65, v68, 16, 16
	v_and_or_b32 v64, v64, s36, v142
	v_lshl_or_b32 v65, v65, 7, v142
	global_load_dwordx4 v[92:95], v64, s[58:59]
	global_load_dwordx4 v[88:91], v65, s[58:59]
	v_lshlrev_b32_e32 v64, 7, v69
	v_bfe_u32 v65, v69, 16, 16
	v_and_or_b32 v64, v64, s36, v142
	v_lshl_or_b32 v65, v65, 7, v142
	global_load_dwordx4 v[84:87], v64, s[58:59]
	global_load_dwordx4 v[80:83], v65, s[58:59]
	v_lshlrev_b32_e32 v64, 7, v70
	v_bfe_u32 v65, v70, 16, 16
	v_and_or_b32 v64, v64, s36, v142
	v_lshl_or_b32 v65, v65, 7, v142
	global_load_dwordx4 v[76:79], v64, s[58:59]
	global_load_dwordx4 v[72:75], v65, s[58:59]
	v_lshlrev_b32_e32 v64, 7, v71
	v_bfe_u32 v65, v71, 16, 16
	v_and_or_b32 v64, v64, s36, v142
	v_lshl_or_b32 v65, v65, 7, v142
	global_load_dwordx4 v[68:71], v64, s[58:59]
	s_nop 0
	global_load_dwordx4 v[64:67], v65, s[58:59]
	s_waitcnt vmcnt(31)
	v_cvt_pk_f32_fp8_e32 v[156:157], v0
	v_cvt_pk_f32_fp8_sdwa v[194:195], v0 src0_sel:WORD_1
	v_cvt_pk_f32_fp8_e32 v[196:197], v1
	v_cvt_pk_f32_fp8_sdwa v[198:199], v1 src0_sel:WORD_1
	v_lshl_add_u32 v128, s30, 9, v164
	s_waitcnt vmcnt(30)
	v_cvt_pk_f32_fp8_e32 v[208:209], v4
	v_cvt_pk_f32_fp8_sdwa v[210:211], v4 src0_sel:WORD_1
	v_cvt_pk_f32_fp8_e32 v[212:213], v5
	v_cvt_pk_f32_fp8_sdwa v[214:215], v5 src0_sel:WORD_1
	ds_read_b128 v[186:189], v128 offset:2048
	ds_read_b128 v[190:193], v128 offset:2064
	ds_read_b128 v[132:135], v128 offset:2080
	ds_read_b128 v[128:131], v128 offset:2096
	v_cvt_pk_f32_fp8_e32 v[200:201], v2
	s_waitcnt lgkmcnt(3)
	v_pk_fma_f32 v[156:157], v[186:187], v[156:157], 0 op_sel_hi:[0,1,0]
	v_pk_fma_f32 v[194:195], v[186:187], v[194:195], 0 op_sel_hi:[0,1,0]
	v_pk_fma_f32 v[196:197], v[186:187], v[196:197], 0 op_sel_hi:[0,1,0]
	v_pk_fma_f32 v[198:199], v[186:187], v[198:199], 0 op_sel_hi:[0,1,0]
	v_cvt_pk_f32_fp8_sdwa v[202:203], v2 src0_sel:WORD_1
	v_cvt_pk_f32_fp8_e32 v[204:205], v3
	v_cvt_pk_f32_fp8_sdwa v[206:207], v3 src0_sel:WORD_1
	v_pk_fma_f32 v[156:157], v[186:187], v[208:209], v[156:157] op_sel:[1,0,0]
	v_pk_fma_f32 v[194:195], v[186:187], v[210:211], v[194:195] op_sel:[1,0,0]
	v_pk_fma_f32 v[196:197], v[186:187], v[212:213], v[196:197] op_sel:[1,0,0]
	v_pk_fma_f32 v[198:199], v[186:187], v[214:215], v[198:199] op_sel:[1,0,0]
	v_cvt_pk_f32_fp8_e32 v[208:209], v6
	v_cvt_pk_f32_fp8_sdwa v[210:211], v6 src0_sel:WORD_1
	v_cvt_pk_f32_fp8_e32 v[212:213], v7
	v_cvt_pk_f32_fp8_sdwa v[214:215], v7 src0_sel:WORD_1
	v_pk_fma_f32 v[200:201], v[186:187], v[200:201], 0 op_sel_hi:[0,1,0]
	v_pk_fma_f32 v[202:203], v[186:187], v[202:203], 0 op_sel_hi:[0,1,0]
	v_pk_fma_f32 v[204:205], v[186:187], v[204:205], 0 op_sel_hi:[0,1,0]
	v_pk_fma_f32 v[206:207], v[186:187], v[206:207], 0 op_sel_hi:[0,1,0]
	v_pk_fma_f32 v[200:201], v[186:187], v[208:209], v[200:201] op_sel:[1,0,0]
	v_pk_fma_f32 v[202:203], v[186:187], v[210:211], v[202:203] op_sel:[1,0,0]
	v_pk_fma_f32 v[204:205], v[186:187], v[212:213], v[204:205] op_sel:[1,0,0]
	v_pk_fma_f32 v[186:187], v[186:187], v[214:215], v[206:207] op_sel:[1,0,0]
	s_waitcnt vmcnt(29)
	v_cvt_pk_f32_fp8_e32 v[206:207], v8
	v_cvt_pk_f32_fp8_sdwa v[208:209], v8 src0_sel:WORD_1
	v_cvt_pk_f32_fp8_e32 v[210:211], v9
	v_cvt_pk_f32_fp8_sdwa v[212:213], v9 src0_sel:WORD_1
	v_pk_fma_f32 v[156:157], v[188:189], v[206:207], v[156:157] op_sel_hi:[0,1,1]
	v_pk_fma_f32 v[194:195], v[188:189], v[208:209], v[194:195] op_sel_hi:[0,1,1]
	v_pk_fma_f32 v[196:197], v[188:189], v[210:211], v[196:197] op_sel_hi:[0,1,1]
	v_pk_fma_f32 v[198:199], v[188:189], v[212:213], v[198:199] op_sel_hi:[0,1,1]
	v_cvt_pk_f32_fp8_e32 v[206:207], v10
	v_cvt_pk_f32_fp8_sdwa v[208:209], v10 src0_sel:WORD_1
	v_cvt_pk_f32_fp8_e32 v[210:211], v11
	v_cvt_pk_f32_fp8_sdwa v[212:213], v11 src0_sel:WORD_1
	v_pk_fma_f32 v[200:201], v[188:189], v[206:207], v[200:201] op_sel_hi:[0,1,1]
	v_pk_fma_f32 v[202:203], v[188:189], v[208:209], v[202:203] op_sel_hi:[0,1,1]
	v_pk_fma_f32 v[204:205], v[188:189], v[210:211], v[204:205] op_sel_hi:[0,1,1]
	v_pk_fma_f32 v[186:187], v[188:189], v[212:213], v[186:187] op_sel_hi:[0,1,1]
	v_mov_b32_e32 v140, v189
	s_waitcnt vmcnt(28)
	v_cvt_pk_f32_fp8_e32 v[188:189], v12
	v_cvt_pk_f32_fp8_sdwa v[206:207], v12 src0_sel:WORD_1
	v_cvt_pk_f32_fp8_e32 v[208:209], v13
	v_cvt_pk_f32_fp8_sdwa v[210:211], v13 src0_sel:WORD_1
	v_pk_fma_f32 v[156:157], v[140:141], v[188:189], v[156:157] op_sel_hi:[0,1,1]
	v_pk_fma_f32 v[188:189], v[140:141], v[206:207], v[194:195] op_sel_hi:[0,1,1]
	v_pk_fma_f32 v[194:195], v[140:141], v[208:209], v[196:197] op_sel_hi:[0,1,1]
	v_pk_fma_f32 v[196:197], v[140:141], v[210:211], v[198:199] op_sel_hi:[0,1,1]
	v_cvt_pk_f32_fp8_e32 v[198:199], v14
	v_cvt_pk_f32_fp8_sdwa v[206:207], v14 src0_sel:WORD_1
	v_cvt_pk_f32_fp8_e32 v[208:209], v15
	v_cvt_pk_f32_fp8_sdwa v[210:211], v15 src0_sel:WORD_1
	v_pk_fma_f32 v[198:199], v[140:141], v[198:199], v[200:201] op_sel_hi:[0,1,1]
	v_pk_fma_f32 v[200:201], v[140:141], v[206:207], v[202:203] op_sel_hi:[0,1,1]
	v_pk_fma_f32 v[202:203], v[140:141], v[208:209], v[204:205] op_sel_hi:[0,1,1]
	v_pk_fma_f32 v[186:187], v[140:141], v[210:211], v[186:187] op_sel_hi:[0,1,1]
	s_waitcnt vmcnt(27)
	v_cvt_pk_f32_fp8_e32 v[204:205], v16
	v_cvt_pk_f32_fp8_sdwa v[206:207], v16 src0_sel:WORD_1
	v_cvt_pk_f32_fp8_e32 v[208:209], v17
	v_cvt_pk_f32_fp8_sdwa v[210:211], v17 src0_sel:WORD_1
	s_waitcnt lgkmcnt(2)
	v_pk_fma_f32 v[156:157], v[190:191], v[204:205], v[156:157] op_sel_hi:[0,1,1]
	v_pk_fma_f32 v[188:189], v[190:191], v[206:207], v[188:189] op_sel_hi:[0,1,1]
	v_pk_fma_f32 v[194:195], v[190:191], v[208:209], v[194:195] op_sel_hi:[0,1,1]
	v_pk_fma_f32 v[196:197], v[190:191], v[210:211], v[196:197] op_sel_hi:[0,1,1]
	v_cvt_pk_f32_fp8_e32 v[204:205], v18
	v_cvt_pk_f32_fp8_sdwa v[206:207], v18 src0_sel:WORD_1
	v_cvt_pk_f32_fp8_e32 v[208:209], v19
	v_cvt_pk_f32_fp8_sdwa v[210:211], v19 src0_sel:WORD_1
	v_pk_fma_f32 v[198:199], v[190:191], v[204:205], v[198:199] op_sel_hi:[0,1,1]
	v_pk_fma_f32 v[200:201], v[190:191], v[206:207], v[200:201] op_sel_hi:[0,1,1]
	v_pk_fma_f32 v[202:203], v[190:191], v[208:209], v[202:203] op_sel_hi:[0,1,1]
	v_pk_fma_f32 v[186:187], v[190:191], v[210:211], v[186:187] op_sel_hi:[0,1,1]
	s_waitcnt vmcnt(26)
	v_cvt_pk_f32_fp8_e32 v[204:205], v20
	v_cvt_pk_f32_fp8_sdwa v[206:207], v20 src0_sel:WORD_1
	v_cvt_pk_f32_fp8_e32 v[208:209], v21
	v_cvt_pk_f32_fp8_sdwa v[210:211], v21 src0_sel:WORD_1
	v_pk_fma_f32 v[156:157], v[190:191], v[204:205], v[156:157] op_sel:[1,0,0]
	v_pk_fma_f32 v[188:189], v[190:191], v[206:207], v[188:189] op_sel:[1,0,0]
	v_pk_fma_f32 v[194:195], v[190:191], v[208:209], v[194:195] op_sel:[1,0,0]
	v_pk_fma_f32 v[196:197], v[190:191], v[210:211], v[196:197] op_sel:[1,0,0]
	v_cvt_pk_f32_fp8_e32 v[204:205], v22
	v_cvt_pk_f32_fp8_sdwa v[206:207], v22 src0_sel:WORD_1
	v_cvt_pk_f32_fp8_e32 v[208:209], v23
	v_cvt_pk_f32_fp8_sdwa v[210:211], v23 src0_sel:WORD_1
	v_pk_fma_f32 v[198:199], v[190:191], v[204:205], v[198:199] op_sel:[1,0,0]
	v_pk_fma_f32 v[200:201], v[190:191], v[206:207], v[200:201] op_sel:[1,0,0]
	v_pk_fma_f32 v[202:203], v[190:191], v[208:209], v[202:203] op_sel:[1,0,0]
	v_pk_fma_f32 v[186:187], v[190:191], v[210:211], v[186:187] op_sel:[1,0,0]
	s_waitcnt vmcnt(25)
	v_cvt_pk_f32_fp8_e32 v[190:191], v24
	v_cvt_pk_f32_fp8_sdwa v[204:205], v24 src0_sel:WORD_1
	v_cvt_pk_f32_fp8_e32 v[206:207], v25
	v_cvt_pk_f32_fp8_sdwa v[208:209], v25 src0_sel:WORD_1
	v_pk_fma_f32 v[156:157], v[192:193], v[190:191], v[156:157] op_sel_hi:[0,1,1]
	v_pk_fma_f32 v[188:189], v[192:193], v[204:205], v[188:189] op_sel_hi:[0,1,1]
	v_pk_fma_f32 v[190:191], v[192:193], v[206:207], v[194:195] op_sel_hi:[0,1,1]
	v_pk_fma_f32 v[194:195], v[192:193], v[208:209], v[196:197] op_sel_hi:[0,1,1]
	v_cvt_pk_f32_fp8_e32 v[196:197], v26
	v_cvt_pk_f32_fp8_sdwa v[204:205], v26 src0_sel:WORD_1
	v_cvt_pk_f32_fp8_e32 v[206:207], v27
	v_cvt_pk_f32_fp8_sdwa v[208:209], v27 src0_sel:WORD_1
	v_pk_fma_f32 v[196:197], v[192:193], v[196:197], v[198:199] op_sel_hi:[0,1,1]
	v_pk_fma_f32 v[198:199], v[192:193], v[204:205], v[200:201] op_sel_hi:[0,1,1]
	v_pk_fma_f32 v[200:201], v[192:193], v[206:207], v[202:203] op_sel_hi:[0,1,1]
	v_pk_fma_f32 v[186:187], v[192:193], v[208:209], v[186:187] op_sel_hi:[0,1,1]
	v_mov_b32_e32 v140, v193
	s_waitcnt vmcnt(24)
	v_cvt_pk_f32_fp8_e32 v[192:193], v28
	v_cvt_pk_f32_fp8_sdwa v[202:203], v28 src0_sel:WORD_1
	v_cvt_pk_f32_fp8_e32 v[204:205], v29
	v_cvt_pk_f32_fp8_sdwa v[206:207], v29 src0_sel:WORD_1
	v_pk_fma_f32 v[156:157], v[140:141], v[192:193], v[156:157] op_sel_hi:[0,1,1]
	v_pk_fma_f32 v[188:189], v[140:141], v[202:203], v[188:189] op_sel_hi:[0,1,1]
	v_pk_fma_f32 v[190:191], v[140:141], v[204:205], v[190:191] op_sel_hi:[0,1,1]
	v_pk_fma_f32 v[192:193], v[140:141], v[206:207], v[194:195] op_sel_hi:[0,1,1]
	v_cvt_pk_f32_fp8_e32 v[194:195], v30
	v_cvt_pk_f32_fp8_sdwa v[202:203], v30 src0_sel:WORD_1
	v_cvt_pk_f32_fp8_e32 v[204:205], v31
	v_cvt_pk_f32_fp8_sdwa v[206:207], v31 src0_sel:WORD_1
	v_pk_fma_f32 v[194:195], v[140:141], v[194:195], v[196:197] op_sel_hi:[0,1,1]
	v_pk_fma_f32 v[196:197], v[140:141], v[202:203], v[198:199] op_sel_hi:[0,1,1]
	v_pk_fma_f32 v[198:199], v[140:141], v[204:205], v[200:201] op_sel_hi:[0,1,1]
	v_pk_fma_f32 v[186:187], v[140:141], v[206:207], v[186:187] op_sel_hi:[0,1,1]
	s_waitcnt vmcnt(23)
	v_cvt_pk_f32_fp8_e32 v[200:201], v32
	v_cvt_pk_f32_fp8_sdwa v[202:203], v32 src0_sel:WORD_1
	v_cvt_pk_f32_fp8_e32 v[204:205], v33
	v_cvt_pk_f32_fp8_sdwa v[206:207], v33 src0_sel:WORD_1
	s_waitcnt lgkmcnt(1)
	v_pk_fma_f32 v[156:157], v[132:133], v[200:201], v[156:157] op_sel_hi:[0,1,1]
	v_pk_fma_f32 v[188:189], v[132:133], v[202:203], v[188:189] op_sel_hi:[0,1,1]
	v_pk_fma_f32 v[190:191], v[132:133], v[204:205], v[190:191] op_sel_hi:[0,1,1]
	v_pk_fma_f32 v[192:193], v[132:133], v[206:207], v[192:193] op_sel_hi:[0,1,1]
	v_cvt_pk_f32_fp8_e32 v[200:201], v34
	v_cvt_pk_f32_fp8_sdwa v[202:203], v34 src0_sel:WORD_1
	v_cvt_pk_f32_fp8_e32 v[204:205], v35
	v_cvt_pk_f32_fp8_sdwa v[206:207], v35 src0_sel:WORD_1
	v_pk_fma_f32 v[194:195], v[132:133], v[200:201], v[194:195] op_sel_hi:[0,1,1]
	v_pk_fma_f32 v[196:197], v[132:133], v[202:203], v[196:197] op_sel_hi:[0,1,1]
	v_pk_fma_f32 v[198:199], v[132:133], v[204:205], v[198:199] op_sel_hi:[0,1,1]
	v_pk_fma_f32 v[186:187], v[132:133], v[206:207], v[186:187] op_sel_hi:[0,1,1]
	s_waitcnt vmcnt(22)
	v_cvt_pk_f32_fp8_e32 v[200:201], v36
	v_cvt_pk_f32_fp8_sdwa v[202:203], v36 src0_sel:WORD_1
	v_cvt_pk_f32_fp8_e32 v[204:205], v37
	v_cvt_pk_f32_fp8_sdwa v[206:207], v37 src0_sel:WORD_1
	v_pk_fma_f32 v[156:157], v[132:133], v[200:201], v[156:157] op_sel:[1,0,0]
	v_pk_fma_f32 v[188:189], v[132:133], v[202:203], v[188:189] op_sel:[1,0,0]
	v_pk_fma_f32 v[190:191], v[132:133], v[204:205], v[190:191] op_sel:[1,0,0]
	v_pk_fma_f32 v[192:193], v[132:133], v[206:207], v[192:193] op_sel:[1,0,0]
	v_cvt_pk_f32_fp8_e32 v[200:201], v38
	v_cvt_pk_f32_fp8_sdwa v[202:203], v38 src0_sel:WORD_1
	v_cvt_pk_f32_fp8_e32 v[204:205], v39
	v_cvt_pk_f32_fp8_sdwa v[206:207], v39 src0_sel:WORD_1
	v_pk_fma_f32 v[194:195], v[132:133], v[200:201], v[194:195] op_sel:[1,0,0]
	v_pk_fma_f32 v[196:197], v[132:133], v[202:203], v[196:197] op_sel:[1,0,0]
	v_pk_fma_f32 v[198:199], v[132:133], v[204:205], v[198:199] op_sel:[1,0,0]
	v_pk_fma_f32 v[132:133], v[132:133], v[206:207], v[186:187] op_sel:[1,0,0]
	s_waitcnt vmcnt(21)
	v_cvt_pk_f32_fp8_e32 v[186:187], v40
	v_cvt_pk_f32_fp8_sdwa v[200:201], v40 src0_sel:WORD_1
	v_cvt_pk_f32_fp8_e32 v[202:203], v41
	v_cvt_pk_f32_fp8_sdwa v[204:205], v41 src0_sel:WORD_1
	v_pk_fma_f32 v[156:157], v[134:135], v[186:187], v[156:157] op_sel_hi:[0,1,1]
	v_pk_fma_f32 v[186:187], v[134:135], v[200:201], v[188:189] op_sel_hi:[0,1,1]
	v_pk_fma_f32 v[188:189], v[134:135], v[202:203], v[190:191] op_sel_hi:[0,1,1]
	v_pk_fma_f32 v[190:191], v[134:135], v[204:205], v[192:193] op_sel_hi:[0,1,1]
	v_cvt_pk_f32_fp8_e32 v[192:193], v42
	v_cvt_pk_f32_fp8_sdwa v[200:201], v42 src0_sel:WORD_1
	v_cvt_pk_f32_fp8_e32 v[202:203], v43
	v_cvt_pk_f32_fp8_sdwa v[204:205], v43 src0_sel:WORD_1
	v_pk_fma_f32 v[192:193], v[134:135], v[192:193], v[194:195] op_sel_hi:[0,1,1]
	v_pk_fma_f32 v[194:195], v[134:135], v[200:201], v[196:197] op_sel_hi:[0,1,1]
	v_pk_fma_f32 v[196:197], v[134:135], v[202:203], v[198:199] op_sel_hi:[0,1,1]
	v_pk_fma_f32 v[132:133], v[134:135], v[204:205], v[132:133] op_sel_hi:[0,1,1]
	s_waitcnt vmcnt(20)
	v_cvt_pk_f32_fp8_e32 v[198:199], v44
	v_cvt_pk_f32_fp8_sdwa v[200:201], v44 src0_sel:WORD_1
	v_cvt_pk_f32_fp8_e32 v[202:203], v45
	v_cvt_pk_f32_fp8_sdwa v[204:205], v45 src0_sel:WORD_1
	v_mov_b32_e32 v134, v135
	v_pk_fma_f32 v[156:157], v[134:135], v[198:199], v[156:157] op_sel_hi:[0,1,1]
	v_pk_fma_f32 v[186:187], v[134:135], v[200:201], v[186:187] op_sel_hi:[0,1,1]
	v_pk_fma_f32 v[188:189], v[134:135], v[202:203], v[188:189] op_sel_hi:[0,1,1]
	v_pk_fma_f32 v[190:191], v[134:135], v[204:205], v[190:191] op_sel_hi:[0,1,1]
	v_cvt_pk_f32_fp8_e32 v[198:199], v46
	v_cvt_pk_f32_fp8_sdwa v[200:201], v46 src0_sel:WORD_1
	v_cvt_pk_f32_fp8_e32 v[202:203], v47
	v_cvt_pk_f32_fp8_sdwa v[204:205], v47 src0_sel:WORD_1
	v_pk_fma_f32 v[192:193], v[134:135], v[198:199], v[192:193] op_sel_hi:[0,1,1]
	v_pk_fma_f32 v[194:195], v[134:135], v[200:201], v[194:195] op_sel_hi:[0,1,1]
	v_pk_fma_f32 v[196:197], v[134:135], v[202:203], v[196:197] op_sel_hi:[0,1,1]
	v_pk_fma_f32 v[132:133], v[134:135], v[204:205], v[132:133] op_sel_hi:[0,1,1]
	s_waitcnt vmcnt(19)
	v_cvt_pk_f32_fp8_e32 v[134:135], v48
	v_cvt_pk_f32_fp8_sdwa v[198:199], v48 src0_sel:WORD_1
	v_cvt_pk_f32_fp8_e32 v[200:201], v49
	v_cvt_pk_f32_fp8_sdwa v[202:203], v49 src0_sel:WORD_1
	s_waitcnt lgkmcnt(0)
; __device__ __forceinline__ void rs16(const float (&d)[16], int bit, int sh1, int sh2, int sh3, float (&out)[2]) {
;     float n8[8], n4[4];
; #pragma unroll
;     for (int m = 0; m < 8; ++m) { const bool up = (bit & sh1) != 0; const float mine = up ? d[8 + m] : d[m], theirs = up ? d[m] : d[8 + m]; n8[m] = mine + __shfl_xor(theirs, sh1); }
	v_pk_fma_f32 v[134:135], v[128:129], v[134:135], v[156:157] op_sel_hi:[0,1,1]
	v_pk_fma_f32 v[156:157], v[128:129], v[198:199], v[186:187] op_sel_hi:[0,1,1]
	v_pk_fma_f32 v[186:187], v[128:129], v[200:201], v[188:189] op_sel_hi:[0,1,1]
	v_pk_fma_f32 v[188:189], v[128:129], v[202:203], v[190:191] op_sel_hi:[0,1,1]
	v_cvt_pk_f32_fp8_e32 v[190:191], v50
	v_cvt_pk_f32_fp8_sdwa v[198:199], v50 src0_sel:WORD_1
	v_cvt_pk_f32_fp8_e32 v[200:201], v51
	v_cvt_pk_f32_fp8_sdwa v[202:203], v51 src0_sel:WORD_1
	v_pk_fma_f32 v[190:191], v[128:129], v[190:191], v[192:193] op_sel_hi:[0,1,1]
	v_pk_fma_f32 v[192:193], v[128:129], v[198:199], v[194:195] op_sel_hi:[0,1,1]
	v_pk_fma_f32 v[194:195], v[128:129], v[200:201], v[196:197] op_sel_hi:[0,1,1]
	v_pk_fma_f32 v[132:133], v[128:129], v[202:203], v[132:133] op_sel_hi:[0,1,1]
	s_waitcnt vmcnt(18)
	v_cvt_pk_f32_fp8_e32 v[196:197], v52
	v_cvt_pk_f32_fp8_sdwa v[198:199], v52 src0_sel:WORD_1
	v_cvt_pk_f32_fp8_e32 v[200:201], v53
	v_cvt_pk_f32_fp8_sdwa v[202:203], v53 src0_sel:WORD_1
	v_pk_fma_f32 v[134:135], v[128:129], v[196:197], v[134:135] op_sel:[1,0,0]
	v_pk_fma_f32 v[156:157], v[128:129], v[198:199], v[156:157] op_sel:[1,0,0]
	v_pk_fma_f32 v[186:187], v[128:129], v[200:201], v[186:187] op_sel:[1,0,0]
	v_pk_fma_f32 v[188:189], v[128:129], v[202:203], v[188:189] op_sel:[1,0,0]
	v_cvt_pk_f32_fp8_e32 v[196:197], v54
	v_cvt_pk_f32_fp8_sdwa v[198:199], v54 src0_sel:WORD_1
	v_cvt_pk_f32_fp8_e32 v[200:201], v55
	v_cvt_pk_f32_fp8_sdwa v[202:203], v55 src0_sel:WORD_1
	v_pk_fma_f32 v[190:191], v[128:129], v[196:197], v[190:191] op_sel:[1,0,0]
	v_pk_fma_f32 v[192:193], v[128:129], v[198:199], v[192:193] op_sel:[1,0,0]
	v_pk_fma_f32 v[194:195], v[128:129], v[200:201], v[194:195] op_sel:[1,0,0]
	v_pk_fma_f32 v[128:129], v[128:129], v[202:203], v[132:133] op_sel:[1,0,0]
	s_waitcnt vmcnt(17)
	v_cvt_pk_f32_fp8_e32 v[132:133], v56
	v_cvt_pk_f32_fp8_sdwa v[196:197], v56 src0_sel:WORD_1
	v_cvt_pk_f32_fp8_e32 v[198:199], v57
	v_cvt_pk_f32_fp8_sdwa v[200:201], v57 src0_sel:WORD_1
	v_pk_fma_f32 v[132:133], v[130:131], v[132:133], v[134:135] op_sel_hi:[0,1,1]
	v_pk_fma_f32 v[134:135], v[130:131], v[196:197], v[156:157] op_sel_hi:[0,1,1]
	v_pk_fma_f32 v[156:157], v[130:131], v[198:199], v[186:187] op_sel_hi:[0,1,1]
	v_pk_fma_f32 v[186:187], v[130:131], v[200:201], v[188:189] op_sel_hi:[0,1,1]
	v_cvt_pk_f32_fp8_e32 v[188:189], v58
	v_cvt_pk_f32_fp8_sdwa v[196:197], v58 src0_sel:WORD_1
	v_cvt_pk_f32_fp8_e32 v[198:199], v59
	v_cvt_pk_f32_fp8_sdwa v[200:201], v59 src0_sel:WORD_1
	v_pk_fma_f32 v[188:189], v[130:131], v[188:189], v[190:191] op_sel_hi:[0,1,1]
	v_pk_fma_f32 v[190:191], v[130:131], v[196:197], v[192:193] op_sel_hi:[0,1,1]
	v_pk_fma_f32 v[192:193], v[130:131], v[198:199], v[194:195] op_sel_hi:[0,1,1]
	s_waitcnt vmcnt(16)
	v_cvt_pk_f32_fp8_e32 v[194:195], v60
	v_pk_fma_f32 v[128:129], v[130:131], v[200:201], v[128:129] op_sel_hi:[0,1,1]
	v_cvt_pk_f32_fp8_sdwa v[196:197], v60 src0_sel:WORD_1
	v_cvt_pk_f32_fp8_e32 v[198:199], v61
	v_cvt_pk_f32_fp8_sdwa v[200:201], v61 src0_sel:WORD_1
	v_mov_b32_e32 v130, v131
	v_pk_fma_f32 v[132:133], v[130:131], v[194:195], v[132:133] op_sel_hi:[0,1,1]
	v_cvt_pk_f32_fp8_e32 v[194:195], v62
	v_pk_fma_f32 v[134:135], v[130:131], v[196:197], v[134:135] op_sel_hi:[0,1,1]
	v_pk_fma_f32 v[156:157], v[130:131], v[198:199], v[156:157] op_sel_hi:[0,1,1]
	v_pk_fma_f32 v[186:187], v[130:131], v[200:201], v[186:187] op_sel_hi:[0,1,1]
	v_cvt_pk_f32_fp8_sdwa v[196:197], v62 src0_sel:WORD_1
	v_cvt_pk_f32_fp8_e32 v[198:199], v63
	v_cvt_pk_f32_fp8_sdwa v[200:201], v63 src0_sel:WORD_1
	v_pk_fma_f32 v[188:189], v[130:131], v[194:195], v[188:189] op_sel_hi:[0,1,1]
	v_pk_fma_f32 v[190:191], v[130:131], v[196:197], v[190:191] op_sel_hi:[0,1,1]
	v_pk_fma_f32 v[192:193], v[130:131], v[198:199], v[192:193] op_sel_hi:[0,1,1]
	v_pk_fma_f32 v[128:129], v[130:131], v[200:201], v[128:129] op_sel_hi:[0,1,1]
	v_cndmask_b32_e64 v131, v132, v188, s[8:9]
	v_cndmask_b32_e64 v130, v188, v132, s[8:9]
	ds_bpermute_b32 v131, v137, v131
	v_cndmask_b32_e64 v132, v133, v189, s[8:9]
	ds_bpermute_b32 v132, v137, v132
	v_cndmask_b32_e64 v140, v134, v190, s[8:9]
	ds_bpermute_b32 v140, v137, v140
	s_waitcnt lgkmcnt(2)
	v_add_f32_e32 v130, v130, v131
	v_cndmask_b32_e64 v131, v189, v133, s[8:9]
	s_waitcnt lgkmcnt(1)
	v_add_f32_e32 v131, v131, v132
	v_cndmask_b32_e64 v132, v190, v134, s[8:9]
	v_cndmask_b32_e64 v134, v135, v191, s[8:9]
	v_cndmask_b32_e64 v133, v191, v135, s[8:9]
	ds_bpermute_b32 v134, v137, v134
	v_cndmask_b32_e64 v135, v156, v192, s[8:9]
	s_waitcnt lgkmcnt(1)
	v_add_f32_e32 v132, v132, v140
	ds_bpermute_b32 v135, v137, v135
	v_cndmask_b32_e64 v140, v157, v193, s[8:9]
	ds_bpermute_b32 v140, v137, v140
	s_waitcnt lgkmcnt(2)
	v_add_f32_e32 v133, v133, v134
	v_cndmask_b32_e64 v134, v192, v156, s[8:9]
	s_waitcnt lgkmcnt(1)
	v_add_f32_e32 v134, v134, v135
	v_cndmask_b32_e64 v135, v193, v157, s[8:9]
	s_waitcnt lgkmcnt(0)
	v_add_f32_e32 v135, v135, v140
	v_cndmask_b32_e64 v140, v128, v186, s[8:9]
	v_cndmask_b32_e64 v128, v186, v128, s[8:9]
	v_cndmask_b32_e64 v155, v187, v129, s[8:9]
	ds_bpermute_b32 v128, v137, v128
	ds_bpermute_b32 v155, v137, v155
	v_cndmask_b32_e64 v129, v129, v187, s[8:9]
	v_cndmask_b32_e64 v156, v130, v134, s[10:11]
	v_cndmask_b32_e64 v130, v134, v130, s[10:11]
	s_waitcnt lgkmcnt(1)
; #define GAS __attribute__((address_space(1)))
; #define LDS_WAIT() asm volatile("s_waitcnt lgkmcnt(0)" ::: "memory")
; __device__ __forceinline__ void peer_block(LAS unsigned char* wl, int tok0, const unsigned char* XQ, const float* XS, const unsigned char* U8, const unsigned char* V8, const float* SU, const float* SV, const int* IDX, const float* GATE, const bf16* HB, float* HO, bf16* X2, const float* wfin, int lan ...
;     ...
;     {   u32x4 bufA[16], bufB[16];
;         PB_LOAD(bufA, V8, 0);
; #pragma unroll 1
;         for (int it = 0; it < 256; it += 2) {
;             PB_LOAD(bufB, V8, it + 1);
;             __builtin_amdgcn_sched_barrier(0);
;             PB_VCOMP(bufA, it);
;             __builtin_amdgcn_sched_barrier(0);
;             if (it + 2 < 256) { PB_LOAD(bufA, V8, it + 2); }
;             __builtin_amdgcn_sched_barrier(0);
;             PB_VCOMP(bufB, it + 1);
;             __builtin_amdgcn_sched_barrier(0);
;     ...
;     LDS_WAIT();
;     asm volatile("s_waitcnt vmcnt(0)" ::: "memory");
;     f32x4 gfin[16];
;     { int lq = lane; asm volatile("" : "+v"(lq));
; #pragma unroll
;     for (int q = 0; q < 16; ++q) gfin[q] = *((const GAS f32x4*)wfin + lq + 64 * q); }
	v_add_f32_e32 v128, v140, v128
	s_waitcnt lgkmcnt(0)
	v_add_f32_e32 v129, v129, v155
	v_cndmask_b32_e64 v134, v135, v131, s[10:11]
	v_cndmask_b32_e64 v131, v131, v135, s[10:11]
	v_cndmask_b32_e64 v135, v132, v128, s[10:11]
	v_cndmask_b32_e64 v140, v133, v129, s[10:11]
	ds_bpermute_b32 v156, v138, v156
	ds_bpermute_b32 v131, v138, v131
	ds_bpermute_b32 v135, v138, v135
	ds_bpermute_b32 v140, v138, v140
	v_cndmask_b32_e64 v128, v128, v132, s[10:11]
	v_cndmask_b32_e64 v129, v129, v133, s[10:11]
	s_waitcnt lgkmcnt(3)
	v_add_f32_e32 v130, v130, v156
	s_waitcnt lgkmcnt(2)
	v_add_f32_e32 v131, v134, v131
	s_waitcnt lgkmcnt(1)
	v_add_f32_e32 v128, v128, v135
	s_waitcnt lgkmcnt(0)
	v_add_f32_e32 v129, v129, v140
	v_cndmask_b32_e64 v132, v130, v128, s[12:13]
	v_cndmask_b32_e64 v133, v131, v129, s[12:13]
	s_or_b32 s30, s30, s2
	ds_bpermute_b32 v132, v136, v132
	ds_bpermute_b32 v133, v136, v133
	s_ashr_i32 s31, s30, 31
	s_and_b32 s57, s53, 0xf80
	s_lshl_b64 s[30:31], s[30:31], 13
	s_add_u32 s30, s64, s30
	s_addc_u32 s31, s65, s31
	s_lshl_b32 s57, s57, 1
	v_cndmask_b32_e64 v128, v128, v130, s[12:13]
	v_cndmask_b32_e64 v129, v129, v131, s[12:13]
	s_add_u32 s30, s30, s57
	s_waitcnt lgkmcnt(1)
	v_add_f32_e32 v128, v128, v132
	s_waitcnt lgkmcnt(0)
	v_add_f32_e32 v129, v129, v133
	s_addc_u32 s31, s31, 0
	v_lshlrev_b32_e32 v140, 1, v142
	v_cvt_pk_bf16_f32 v130, v128, v129
	v_lshl_add_u64 v[128:129], s[30:31], 0, v[140:141]
	v_mov_b32_e32 v155, v141
	v_lshl_add_u64 v[128:129], v[128:129], 0, v[154:155]
	global_store_dword v[128:129], v130, off
	s_cmpk_gt_u32 s54, 0xfd
	s_cselect_b64 s[30:31], -1, 0
	s_and_b64 vcc, exec, s[30:31]
	v_and_or_b32 v0, s3, 48, v158
	v_lshl_add_u32 v0, v0, 5, s34
	ds_read_b128 v[22:25], v0
	ds_read_b128 v[54:57], v0 offset:16
	s_and_b32 s57, s22, 0x7e00000
	s_add_u32 s58, s14, s57
	s_addc_u32 s59, s15, 0
	s_waitcnt lgkmcnt(1)
	v_lshlrev_b32_e32 v0, 7, v22
	v_bfe_u32 v1, v22, 16, 16
	v_lshlrev_b32_e32 v8, 7, v23
	v_bfe_u32 v9, v23, 16, 16
	v_lshlrev_b32_e32 v16, 7, v24
	v_bfe_u32 v17, v24, 16, 16
	v_lshlrev_b32_e32 v24, 7, v25
	v_bfe_u32 v25, v25, 16, 16
	s_waitcnt lgkmcnt(0)
	v_lshlrev_b32_e32 v32, 7, v54
	v_bfe_u32 v33, v54, 16, 16
	v_lshlrev_b32_e32 v40, 7, v55
	v_bfe_u32 v41, v55, 16, 16
	v_lshlrev_b32_e32 v48, 7, v56
	v_bfe_u32 v49, v56, 16, 16
	v_lshlrev_b32_e32 v56, 7, v57
	v_bfe_u32 v57, v57, 16, 16
	v_and_or_b32 v0, v0, s36, v142
	v_lshl_or_b32 v4, v1, 7, v142
	v_and_or_b32 v8, v8, s36, v142
	v_lshl_or_b32 v12, v9, 7, v142
	v_and_or_b32 v16, v16, s36, v142
	v_lshl_or_b32 v20, v17, 7, v142
	v_and_or_b32 v24, v24, s36, v142
	v_lshl_or_b32 v28, v25, 7, v142
	v_and_or_b32 v32, v32, s36, v142
	v_lshl_or_b32 v36, v33, 7, v142
	v_and_or_b32 v40, v40, s36, v142
	v_lshl_or_b32 v44, v41, 7, v142
	v_and_or_b32 v48, v48, s36, v142
	v_lshl_or_b32 v52, v49, 7, v142
	v_and_or_b32 v56, v56, s36, v142
	v_lshl_or_b32 v60, v57, 7, v142
	global_load_dwordx4 v[0:3], v0, s[58:59]
	s_nop 0
	global_load_dwordx4 v[4:7], v4, s[58:59]
	s_nop 0
	global_load_dwordx4 v[8:11], v8, s[58:59]
	s_nop 0
	global_load_dwordx4 v[12:15], v12, s[58:59]
	s_nop 0
	global_load_dwordx4 v[16:19], v16, s[58:59]
	s_nop 0
	global_load_dwordx4 v[20:23], v20, s[58:59]
	s_nop 0
	global_load_dwordx4 v[24:27], v24, s[58:59]
	s_nop 0
	global_load_dwordx4 v[28:31], v28, s[58:59]
	s_nop 0
	global_load_dwordx4 v[32:35], v32, s[58:59]
	s_nop 0
	global_load_dwordx4 v[36:39], v36, s[58:59]
	s_nop 0
	global_load_dwordx4 v[40:43], v40, s[58:59]
	s_nop 0
	global_load_dwordx4 v[44:47], v44, s[58:59]
	s_nop 0
	global_load_dwordx4 v[48:51], v48, s[58:59]
	s_nop 0
	global_load_dwordx4 v[52:55], v52, s[58:59]
	s_nop 0
	global_load_dwordx4 v[56:59], v56, s[58:59]
	s_nop 0
	global_load_dwordx4 v[60:63], v60, s[58:59]
	s_branch .LBB0_838
.LBB0_841:
	s_waitcnt vmcnt(0)
	s_waitcnt lgkmcnt(0)
	v_mov_b32_e32 v0, v182
	s_waitcnt vmcnt(0)
	s_lshl_b64 s[2:3], s[24:25], 14
	v_ashrrev_i32_e32 v1, 31, v0
	v_lshl_add_u64 v[48:49], v[0:1], 4, s[66:67]
	v_add_co_u32_e32 v28, vcc, 0x1000, v48
	global_load_dwordx4 v[0:3], v[48:49], off
	global_load_dwordx4 v[4:7], v[48:49], off offset:1024
	global_load_dwordx4 v[8:11], v[48:49], off offset:2048
	global_load_dwordx4 v[12:15], v[48:49], off offset:3072
	v_addc_co_u32_e32 v29, vcc, 0, v49, vcc
	v_add_co_u32_e32 v44, vcc, 0x2000, v48
	global_load_dwordx4 v[16:19], v[28:29], off
	global_load_dwordx4 v[20:23], v[28:29], off offset:1024
	global_load_dwordx4 v[24:27], v[28:29], off offset:2048
	s_nop 0
	global_load_dwordx4 v[28:31], v[28:29], off offset:3072
	v_addc_co_u32_e32 v45, vcc, 0, v49, vcc
	s_waitcnt vmcnt(9)
	v_add_co_u32_e32 v60, vcc, 0x3000, v48
	global_load_dwordx4 v[32:35], v[44:45], off
	global_load_dwordx4 v[36:39], v[44:45], off offset:1024
	global_load_dwordx4 v[40:43], v[44:45], off offset:2048
	s_nop 0
	global_load_dwordx4 v[44:47], v[44:45], off offset:3072
	v_addc_co_u32_e32 v61, vcc, 0, v49, vcc
	global_load_dwordx4 v[48:51], v[60:61], off
	global_load_dwordx4 v[52:55], v[60:61], off offset:1024
	global_load_dwordx4 v[56:59], v[60:61], off offset:2048
	s_nop 0
	global_load_dwordx4 v[60:63], v[60:61], off offset:3072
	v_lshl_add_u64 v[64:65], v[150:151], 0, s[2:3]
	s_lshl_b64 s[2:3], s[24:25], 13
	v_lshl_add_u64 v[66:67], v[152:153], 0, s[2:3]
	s_mov_b64 s[30:31], 0
